# baseline (speedup 1.0000x reference)
.LBB0_33:
	s_cmp_lg_u64 s[4:5], 0
	s_cbranch_scc0 .Ltail_noprio
	s_setprio 1
